# q6 + phase-A converter budget 5.5 grabs instead of 5
# baseline (speedup 1.0000x reference)
.LBB0_181:
	s_mul_i32 s6, s90, 0xd760
	s_max_i32 s57, s50, s6
	s_sub_i32 s86, s25, s92
	s_and_b64 s[6:7], s[2:3], exec
	s_movk_i32 s4, 0x80
	s_cselect_b32 s6, s4, 0x160
	s_mul_i32 s6, s6, s86
	s_add_i32 s6, s6, s57
	s_min_i32 s50, s6, 0x34920
	s_cmp_lt_i32 s89, 0
	s_mov_b64 s[6:7], -1
	s_cbranch_scc0 .LBB0_712
	s_andn2_b64 vcc, exec, s[2:3]
	s_not_b32 s68, s89
	s_cbranch_vccnz .LBB0_260
	s_add_u32 s26, s52, 0x37200000
	s_addc_u32 s27, s53, 0
	s_add_u32 s28, s52, 0x5200000
	s_addc_u32 s29, s53, 0
	s_waitcnt vmcnt(0)
	v_mov_b32_e32 v1, v0
	s_cmp_gt_u32 s89, 0xffffffdf
	s_cselect_b64 s[6:7], -1, 0
	s_cmp_lt_u32 s89, 0xffffffe0
	v_readfirstlane_b32 s3, v1
	s_cbranch_scc1 .LBB0_185
	s_lshr_b32 s8, s68, 3
	s_and_b32 s2, s68, 7
	s_lshl_b32 s9, s8, 20
	s_add_u32 s18, s26, s9
	s_addc_u32 s19, s27, 0
	s_lshl_b32 s9, s2, 20
	s_add_u32 s20, s28, s9
	s_addc_u32 s21, s29, 0
	s_lshl_b32 s30, s8, 8
	s_lshl_b32 s2, s2, 8
